# selected-attention block epilogue through the LDS tile as well; 36864 conversion items beside it
# speedup vs baseline: 1.0235x; 1.0048x over previous
.LBB0_862:
	s_waitcnt vmcnt(8)
	s_waitcnt vmcnt(9)
	ds_write_b128 v222, v[98:101] offset:32768
	s_waitcnt vmcnt(8)
	ds_write_b128 v222, v[102:105] offset:40960
	s_and_saveexec_b64 s[8:9], s[4:5]
	ds_write_b32 v224, v114
	s_or_b64 exec, exec, s[8:9]
	s_waitcnt lgkmcnt(0)
	ds_read_b128 v[66:69], v205
	ds_read_b128 v[70:73], v205 offset:32
	ds_read_b128 v[74:77], v205 offset:64
	ds_read_b128 v[78:81], v205 offset:96
	s_add_u32 s0, s26, s28
	s_addc_u32 s1, s27, s29
	s_lshl_b32 s2, s47, 12
	s_add_u32 s0, s0, s2
	s_addc_u32 s1, s1, 0
	v_lshrrev_b32_e32 v82, 6, v254
	v_lshlrev_b32_e32 v82, 13, v82
	v_add_u32_e32 v82, 0x11000, v82
	v_and_b32_e32 v83, 31, v214
	v_lshrrev_b32_e32 v84, 5, v214
	v_lshlrev_b32_e32 v83, 1, v83
	v_lshl_add_u32 v83, v84, 10, v83
	v_add_u32_e32 v83, v82, v83
	v_lshl_add_u32 v82, v214, 4, v82
	v_lshrrev_b32_e32 v84, 4, v214
	v_and_b32_e32 v85, 15, v214
	v_lshlrev_b32_e32 v85, 4, v85
	v_lshl_add_u32 v84, v84, 12, v85
	s_waitcnt lgkmcnt(0)
	v_rcp_f32_e32 v66, v66
	v_rcp_f32_e32 v67, v67
	v_rcp_f32_e32 v68, v68
	v_rcp_f32_e32 v69, v69
	v_rcp_f32_e32 v70, v70
	v_rcp_f32_e32 v71, v71
	v_rcp_f32_e32 v72, v72
	v_rcp_f32_e32 v73, v73
	v_rcp_f32_e32 v74, v74
	v_rcp_f32_e32 v75, v75
	v_rcp_f32_e32 v76, v76
	v_rcp_f32_e32 v77, v77
	v_rcp_f32_e32 v78, v78
	v_rcp_f32_e32 v79, v79
	v_rcp_f32_e32 v80, v80
	v_rcp_f32_e32 v81, v81
	v_mul_f32_e32 v50, v50, v66
	v_mul_f32_e32 v34, v34, v66
	v_mul_f32_e32 v18, v18, v66
	v_mul_f32_e32 v2, v2, v66
	v_mul_f32_e32 v51, v51, v67
	v_mul_f32_e32 v35, v35, v67
	v_mul_f32_e32 v19, v19, v67
	v_mul_f32_e32 v3, v3, v67
	v_mov_b32_dpp v114, v50 quad_perm:[1,0,3,2] row_mask:0xf bank_mask:0xf
	v_mov_b32_dpp v115, v34 quad_perm:[1,0,3,2] row_mask:0xf bank_mask:0xf
	v_mov_b32_dpp v116, v18 quad_perm:[1,0,3,2] row_mask:0xf bank_mask:0xf
	v_mov_b32_dpp v117, v2 quad_perm:[1,0,3,2] row_mask:0xf bank_mask:0xf
	v_mov_b32_dpp v118, v51 quad_perm:[1,0,3,2] row_mask:0xf bank_mask:0xf
	v_mov_b32_dpp v119, v35 quad_perm:[1,0,3,2] row_mask:0xf bank_mask:0xf
	v_mov_b32_dpp v120, v19 quad_perm:[1,0,3,2] row_mask:0xf bank_mask:0xf
	v_mov_b32_dpp v121, v3 quad_perm:[1,0,3,2] row_mask:0xf bank_mask:0xf
	v_cvt_pk_bf16_f32 v50, v50, v114
	v_cvt_pk_bf16_f32 v34, v34, v115
	v_cvt_pk_bf16_f32 v18, v18, v116
	v_cvt_pk_bf16_f32 v2, v2, v117
	v_cvt_pk_bf16_f32 v51, v51, v118
	v_cvt_pk_bf16_f32 v35, v35, v119
	v_cvt_pk_bf16_f32 v19, v19, v120
	v_cvt_pk_bf16_f32 v3, v3, v121
	v_mul_f32_e32 v52, v52, v68
	v_mul_f32_e32 v36, v36, v68
	v_mul_f32_e32 v20, v20, v68
	v_mul_f32_e32 v4, v4, v68
	v_mul_f32_e32 v53, v53, v69
	v_mul_f32_e32 v37, v37, v69
	v_mul_f32_e32 v21, v21, v69
	v_mul_f32_e32 v5, v5, v69
	v_mov_b32_dpp v114, v52 quad_perm:[1,0,3,2] row_mask:0xf bank_mask:0xf
	v_mov_b32_dpp v115, v36 quad_perm:[1,0,3,2] row_mask:0xf bank_mask:0xf
	v_mov_b32_dpp v116, v20 quad_perm:[1,0,3,2] row_mask:0xf bank_mask:0xf
	v_mov_b32_dpp v117, v4 quad_perm:[1,0,3,2] row_mask:0xf bank_mask:0xf
	v_mov_b32_dpp v118, v53 quad_perm:[1,0,3,2] row_mask:0xf bank_mask:0xf
	v_mov_b32_dpp v119, v37 quad_perm:[1,0,3,2] row_mask:0xf bank_mask:0xf
	v_mov_b32_dpp v120, v21 quad_perm:[1,0,3,2] row_mask:0xf bank_mask:0xf
	v_mov_b32_dpp v121, v5 quad_perm:[1,0,3,2] row_mask:0xf bank_mask:0xf
	v_cvt_pk_bf16_f32 v52, v52, v114
	v_cvt_pk_bf16_f32 v36, v36, v115
	v_cvt_pk_bf16_f32 v20, v20, v116
	v_cvt_pk_bf16_f32 v4, v4, v117
	v_cvt_pk_bf16_f32 v53, v53, v118
	v_cvt_pk_bf16_f32 v37, v37, v119
	v_cvt_pk_bf16_f32 v21, v21, v120
	v_cvt_pk_bf16_f32 v5, v5, v121
	v_mul_f32_e32 v54, v54, v70
	v_mul_f32_e32 v38, v38, v70
	v_mul_f32_e32 v22, v22, v70
	v_mul_f32_e32 v6, v6, v70
	v_mul_f32_e32 v55, v55, v71
	v_mul_f32_e32 v39, v39, v71
	v_mul_f32_e32 v23, v23, v71
	v_mul_f32_e32 v7, v7, v71
	v_mov_b32_dpp v114, v54 quad_perm:[1,0,3,2] row_mask:0xf bank_mask:0xf
	v_mov_b32_dpp v115, v38 quad_perm:[1,0,3,2] row_mask:0xf bank_mask:0xf
	v_mov_b32_dpp v116, v22 quad_perm:[1,0,3,2] row_mask:0xf bank_mask:0xf
	v_mov_b32_dpp v117, v6 quad_perm:[1,0,3,2] row_mask:0xf bank_mask:0xf
	v_mov_b32_dpp v118, v55 quad_perm:[1,0,3,2] row_mask:0xf bank_mask:0xf
	v_mov_b32_dpp v119, v39 quad_perm:[1,0,3,2] row_mask:0xf bank_mask:0xf
	v_mov_b32_dpp v120, v23 quad_perm:[1,0,3,2] row_mask:0xf bank_mask:0xf
	v_mov_b32_dpp v121, v7 quad_perm:[1,0,3,2] row_mask:0xf bank_mask:0xf
	v_cvt_pk_bf16_f32 v54, v54, v114
	v_cvt_pk_bf16_f32 v38, v38, v115
	v_cvt_pk_bf16_f32 v22, v22, v116
	v_cvt_pk_bf16_f32 v6, v6, v117
	v_cvt_pk_bf16_f32 v55, v55, v118
	v_cvt_pk_bf16_f32 v39, v39, v119
	v_cvt_pk_bf16_f32 v23, v23, v120
	v_cvt_pk_bf16_f32 v7, v7, v121
	v_mul_f32_e32 v56, v56, v72
	v_mul_f32_e32 v40, v40, v72
	v_mul_f32_e32 v24, v24, v72
	v_mul_f32_e32 v8, v8, v72
	v_mul_f32_e32 v57, v57, v73
	v_mul_f32_e32 v41, v41, v73
	v_mul_f32_e32 v25, v25, v73
	v_mul_f32_e32 v9, v9, v73
	v_mov_b32_dpp v114, v56 quad_perm:[1,0,3,2] row_mask:0xf bank_mask:0xf
	v_mov_b32_dpp v115, v40 quad_perm:[1,0,3,2] row_mask:0xf bank_mask:0xf
	v_mov_b32_dpp v116, v24 quad_perm:[1,0,3,2] row_mask:0xf bank_mask:0xf
	v_mov_b32_dpp v117, v8 quad_perm:[1,0,3,2] row_mask:0xf bank_mask:0xf
	v_mov_b32_dpp v118, v57 quad_perm:[1,0,3,2] row_mask:0xf bank_mask:0xf
	v_mov_b32_dpp v119, v41 quad_perm:[1,0,3,2] row_mask:0xf bank_mask:0xf
	v_mov_b32_dpp v120, v25 quad_perm:[1,0,3,2] row_mask:0xf bank_mask:0xf
	v_mov_b32_dpp v121, v9 quad_perm:[1,0,3,2] row_mask:0xf bank_mask:0xf
	v_cvt_pk_bf16_f32 v56, v56, v114
	v_cvt_pk_bf16_f32 v40, v40, v115
	v_cvt_pk_bf16_f32 v24, v24, v116
	v_cvt_pk_bf16_f32 v8, v8, v117
	v_cvt_pk_bf16_f32 v57, v57, v118
	v_cvt_pk_bf16_f32 v41, v41, v119
	v_cvt_pk_bf16_f32 v25, v25, v120
	v_cvt_pk_bf16_f32 v9, v9, v121
	v_mul_f32_e32 v58, v58, v74
	v_mul_f32_e32 v42, v42, v74
	v_mul_f32_e32 v26, v26, v74
	v_mul_f32_e32 v10, v10, v74
	v_mul_f32_e32 v59, v59, v75
	v_mul_f32_e32 v43, v43, v75
	v_mul_f32_e32 v27, v27, v75
	v_mul_f32_e32 v11, v11, v75
	v_mov_b32_dpp v114, v58 quad_perm:[1,0,3,2] row_mask:0xf bank_mask:0xf
	v_mov_b32_dpp v115, v42 quad_perm:[1,0,3,2] row_mask:0xf bank_mask:0xf
	v_mov_b32_dpp v116, v26 quad_perm:[1,0,3,2] row_mask:0xf bank_mask:0xf
	v_mov_b32_dpp v117, v10 quad_perm:[1,0,3,2] row_mask:0xf bank_mask:0xf
	v_mov_b32_dpp v118, v59 quad_perm:[1,0,3,2] row_mask:0xf bank_mask:0xf
	v_mov_b32_dpp v119, v43 quad_perm:[1,0,3,2] row_mask:0xf bank_mask:0xf
	v_mov_b32_dpp v120, v27 quad_perm:[1,0,3,2] row_mask:0xf bank_mask:0xf
	v_mov_b32_dpp v121, v11 quad_perm:[1,0,3,2] row_mask:0xf bank_mask:0xf
	v_cvt_pk_bf16_f32 v58, v58, v114
	v_cvt_pk_bf16_f32 v42, v42, v115
	v_cvt_pk_bf16_f32 v26, v26, v116
	v_cvt_pk_bf16_f32 v10, v10, v117
	v_cvt_pk_bf16_f32 v59, v59, v118
	v_cvt_pk_bf16_f32 v43, v43, v119
	v_cvt_pk_bf16_f32 v27, v27, v120
	v_cvt_pk_bf16_f32 v11, v11, v121
	v_mul_f32_e32 v60, v60, v76
	v_mul_f32_e32 v44, v44, v76
	v_mul_f32_e32 v28, v28, v76
	v_mul_f32_e32 v12, v12, v76
	v_mul_f32_e32 v61, v61, v77
	v_mul_f32_e32 v45, v45, v77
	v_mul_f32_e32 v29, v29, v77
	v_mul_f32_e32 v13, v13, v77
	v_mov_b32_dpp v114, v60 quad_perm:[1,0,3,2] row_mask:0xf bank_mask:0xf
	v_mov_b32_dpp v115, v44 quad_perm:[1,0,3,2] row_mask:0xf bank_mask:0xf
	v_mov_b32_dpp v116, v28 quad_perm:[1,0,3,2] row_mask:0xf bank_mask:0xf
	v_mov_b32_dpp v117, v12 quad_perm:[1,0,3,2] row_mask:0xf bank_mask:0xf
	v_mov_b32_dpp v118, v61 quad_perm:[1,0,3,2] row_mask:0xf bank_mask:0xf
	v_mov_b32_dpp v119, v45 quad_perm:[1,0,3,2] row_mask:0xf bank_mask:0xf
	v_mov_b32_dpp v120, v29 quad_perm:[1,0,3,2] row_mask:0xf bank_mask:0xf
	v_mov_b32_dpp v121, v13 quad_perm:[1,0,3,2] row_mask:0xf bank_mask:0xf
	v_cvt_pk_bf16_f32 v60, v60, v114
	v_cvt_pk_bf16_f32 v44, v44, v115
	v_cvt_pk_bf16_f32 v28, v28, v116
	v_cvt_pk_bf16_f32 v12, v12, v117
	v_cvt_pk_bf16_f32 v61, v61, v118
	v_cvt_pk_bf16_f32 v45, v45, v119
	v_cvt_pk_bf16_f32 v29, v29, v120
	v_cvt_pk_bf16_f32 v13, v13, v121
	v_mul_f32_e32 v62, v62, v78
	v_mul_f32_e32 v46, v46, v78
	v_mul_f32_e32 v30, v30, v78
	v_mul_f32_e32 v14, v14, v78
	v_mul_f32_e32 v63, v63, v79
	v_mul_f32_e32 v47, v47, v79
	v_mul_f32_e32 v31, v31, v79
	v_mul_f32_e32 v15, v15, v79
	v_mov_b32_dpp v114, v62 quad_perm:[1,0,3,2] row_mask:0xf bank_mask:0xf
	v_mov_b32_dpp v115, v46 quad_perm:[1,0,3,2] row_mask:0xf bank_mask:0xf
	v_mov_b32_dpp v116, v30 quad_perm:[1,0,3,2] row_mask:0xf bank_mask:0xf
	v_mov_b32_dpp v117, v14 quad_perm:[1,0,3,2] row_mask:0xf bank_mask:0xf
	v_mov_b32_dpp v118, v63 quad_perm:[1,0,3,2] row_mask:0xf bank_mask:0xf
	v_mov_b32_dpp v119, v47 quad_perm:[1,0,3,2] row_mask:0xf bank_mask:0xf
	v_mov_b32_dpp v120, v31 quad_perm:[1,0,3,2] row_mask:0xf bank_mask:0xf
	v_mov_b32_dpp v121, v15 quad_perm:[1,0,3,2] row_mask:0xf bank_mask:0xf
	v_cvt_pk_bf16_f32 v62, v62, v114
	v_cvt_pk_bf16_f32 v46, v46, v115
	v_cvt_pk_bf16_f32 v30, v30, v116
	v_cvt_pk_bf16_f32 v14, v14, v117
	v_cvt_pk_bf16_f32 v63, v63, v118
	v_cvt_pk_bf16_f32 v47, v47, v119
	v_cvt_pk_bf16_f32 v31, v31, v120
	v_cvt_pk_bf16_f32 v15, v15, v121
	v_mul_f32_e32 v64, v64, v80
	v_mul_f32_e32 v48, v48, v80
	v_mul_f32_e32 v32, v32, v80
	v_mul_f32_e32 v16, v16, v80
	v_mul_f32_e32 v65, v65, v81
	v_mul_f32_e32 v49, v49, v81
	v_mul_f32_e32 v33, v33, v81
	v_mul_f32_e32 v17, v17, v81
	v_mov_b32_dpp v114, v64 quad_perm:[1,0,3,2] row_mask:0xf bank_mask:0xf
	v_mov_b32_dpp v115, v48 quad_perm:[1,0,3,2] row_mask:0xf bank_mask:0xf
	v_mov_b32_dpp v116, v32 quad_perm:[1,0,3,2] row_mask:0xf bank_mask:0xf
	v_mov_b32_dpp v117, v16 quad_perm:[1,0,3,2] row_mask:0xf bank_mask:0xf
	v_mov_b32_dpp v118, v65 quad_perm:[1,0,3,2] row_mask:0xf bank_mask:0xf
	v_mov_b32_dpp v119, v49 quad_perm:[1,0,3,2] row_mask:0xf bank_mask:0xf
	v_mov_b32_dpp v120, v33 quad_perm:[1,0,3,2] row_mask:0xf bank_mask:0xf
	v_mov_b32_dpp v121, v17 quad_perm:[1,0,3,2] row_mask:0xf bank_mask:0xf
	v_cvt_pk_bf16_f32 v64, v64, v114
	v_cvt_pk_bf16_f32 v48, v48, v115
	v_cvt_pk_bf16_f32 v32, v32, v116
	v_cvt_pk_bf16_f32 v16, v16, v117
	v_cvt_pk_bf16_f32 v65, v65, v118
	v_cvt_pk_bf16_f32 v49, v49, v119
	v_cvt_pk_bf16_f32 v33, v33, v120
	v_cvt_pk_bf16_f32 v17, v17, v121
	s_mov_b64 s[100:101], exec
	s_and_b64 exec, exec, s[6:7]
	ds_write_b32 v83, v50
	ds_write_b32 v83, v34 offset:64
	ds_write_b32 v83, v18 offset:128
	ds_write_b32 v83, v2 offset:192
	ds_write_b32 v83, v51 offset:256
	ds_write_b32 v83, v35 offset:320
	ds_write_b32 v83, v19 offset:384
	ds_write_b32 v83, v3 offset:448
	ds_write_b32 v83, v52 offset:512
	ds_write_b32 v83, v36 offset:576
	ds_write_b32 v83, v20 offset:640
	ds_write_b32 v83, v4 offset:704
	ds_write_b32 v83, v53 offset:768
	ds_write_b32 v83, v37 offset:832
	ds_write_b32 v83, v21 offset:896
	ds_write_b32 v83, v5 offset:960
	ds_write_b32 v83, v54 offset:2048
	ds_write_b32 v83, v38 offset:2112
	ds_write_b32 v83, v22 offset:2176
	ds_write_b32 v83, v6 offset:2240
	ds_write_b32 v83, v55 offset:2304
	ds_write_b32 v83, v39 offset:2368
	ds_write_b32 v83, v23 offset:2432
	ds_write_b32 v83, v7 offset:2496
	ds_write_b32 v83, v56 offset:2560
	ds_write_b32 v83, v40 offset:2624
	ds_write_b32 v83, v24 offset:2688
	ds_write_b32 v83, v8 offset:2752
	ds_write_b32 v83, v57 offset:2816
	ds_write_b32 v83, v41 offset:2880
	ds_write_b32 v83, v25 offset:2944
	ds_write_b32 v83, v9 offset:3008
	ds_write_b32 v83, v58 offset:4096
	ds_write_b32 v83, v42 offset:4160
	ds_write_b32 v83, v26 offset:4224
	ds_write_b32 v83, v10 offset:4288
	ds_write_b32 v83, v59 offset:4352
	ds_write_b32 v83, v43 offset:4416
	ds_write_b32 v83, v27 offset:4480
	ds_write_b32 v83, v11 offset:4544
	ds_write_b32 v83, v60 offset:4608
	ds_write_b32 v83, v44 offset:4672
	ds_write_b32 v83, v28 offset:4736
	ds_write_b32 v83, v12 offset:4800
	ds_write_b32 v83, v61 offset:4864
	ds_write_b32 v83, v45 offset:4928
	ds_write_b32 v83, v29 offset:4992
	ds_write_b32 v83, v13 offset:5056
	ds_write_b32 v83, v62 offset:6144
	ds_write_b32 v83, v46 offset:6208
	ds_write_b32 v83, v30 offset:6272
	ds_write_b32 v83, v14 offset:6336
	ds_write_b32 v83, v63 offset:6400
	ds_write_b32 v83, v47 offset:6464
	ds_write_b32 v83, v31 offset:6528
	ds_write_b32 v83, v15 offset:6592
	ds_write_b32 v83, v64 offset:6656
	ds_write_b32 v83, v48 offset:6720
	ds_write_b32 v83, v32 offset:6784
	ds_write_b32 v83, v16 offset:6848
	ds_write_b32 v83, v65 offset:6912
	ds_write_b32 v83, v49 offset:6976
	ds_write_b32 v83, v33 offset:7040
	ds_write_b32 v83, v17 offset:7104
	s_mov_b64 exec, s[100:101]
	ds_read_b128 v[66:69], v82
	ds_read_b128 v[70:73], v82 offset:1024
	ds_read_b128 v[74:77], v82 offset:2048
	ds_read_b128 v[78:81], v82 offset:3072
	ds_read_b128 v[86:89], v82 offset:4096
	ds_read_b128 v[90:93], v82 offset:5120
	ds_read_b128 v[94:97], v82 offset:6144
	ds_read_b128 v[98:101], v82 offset:7168
	s_waitcnt lgkmcnt(7)
	global_store_dwordx4 v84, v[66:69], s[0:1]
	s_waitcnt lgkmcnt(6)
	v_add_u32_e32 v85, 16384, v84
	global_store_dwordx4 v85, v[70:73], s[0:1]
	s_waitcnt lgkmcnt(5)
	v_add_u32_e32 v85, 32768, v84
	global_store_dwordx4 v85, v[74:77], s[0:1]
	s_waitcnt lgkmcnt(4)
	v_add_u32_e32 v85, 49152, v84
	global_store_dwordx4 v85, v[78:81], s[0:1]
	s_waitcnt lgkmcnt(3)
	v_add_u32_e32 v85, 65536, v84
	global_store_dwordx4 v85, v[86:89], s[0:1]
	s_waitcnt lgkmcnt(2)
	v_add_u32_e32 v85, 81920, v84
	global_store_dwordx4 v85, v[90:93], s[0:1]
	s_waitcnt lgkmcnt(1)
	v_add_u32_e32 v85, 98304, v84
	global_store_dwordx4 v85, v[94:97], s[0:1]
	s_waitcnt lgkmcnt(0)
	v_add_u32_e32 v85, 114688, v84
	global_store_dwordx4 v85, v[98:101], s[0:1]
	s_branch .LBB0_819
